# speedup vs baseline: 1.0164x; 1.0018x over previous
.Lstag_done_p1:
	s_lshr_b32 s22, s2, 3
	s_sub_i32 s22, 0xbf, s22
	s_and_b32 s2, s2, 7
	s_lshl_b32 s22, s22, 3
	s_or_b32 s2, s2, s22
	s_ashr_i32 s15, s2, 3
	s_mul_hi_i32 s14, s15, 0x55555556
	s_lshr_b32 s12, s14, 31
	s_add_i32 s14, s14, s12
	s_mul_i32 s16, s14, 0x3fffffd
	s_add_i32 s16, s16, s15
	s_lshl_b32 s15, s16, 6
	s_lshl_b32 s16, s2, 5
	s_and_b32 s16, s16, 32
	s_or_b32 s15, s15, s16
	s_bfe_u32 s16, s2, 0x20001
	s_mul_i32 s2, s16, 0xc0
	s_lshl_b32 s12, s14, 1
	s_add_i32 s17, s15, s2
	s_load_dwordx8 s[4:11], s[0:1], 0x0
	s_and_b32 s12, s12, -16
	s_lshl_b32 s13, s14, 4
	s_and_b32 s13, s13, 0x70
	s_mov_b32 s3, 0
	v_mov_b32_e32 v32, 0
	v_lshrrev_b32_e32 v78, 6, v0
	v_bfe_u32 v65, v0, 2, 4
	v_lshlrev_b32_e32 v1, 4, v0
	v_and_b32_e32 v30, 48, v1
	v_lshl_add_u32 v1, v78, 7, v65
	v_lshl_add_u32 v1, v1, 9, v30
	s_lshl_b32 s18, s17, 7
	s_add_i32 s18, s18, s12
	s_lshl_b32 s18, s18, 9
	s_lshl_b32 s2, s13, 2
	s_add_i32 s18, s18, s2
	s_waitcnt lgkmcnt(0)
	s_add_u32 s20, s4, s18
	s_addc_u32 s21, s5, 0
	s_add_u32 s22, s20, 0x40000
	s_addc_u32 s23, s21, 0
	s_add_u32 s24, s22, 0x40000
	s_addc_u32 s25, s23, 0
	s_add_u32 s26, s24, 0x40000
	s_addc_u32 s27, s25, 0
	s_add_u32 s28, s26, 0x40000
	s_addc_u32 s29, s27, 0
	s_add_u32 s30, s28, 0x40000
	s_addc_u32 s31, s29, 0
	s_add_u32 s32, s30, 0x40000
	s_addc_u32 s33, s31, 0
	s_add_u32 s34, s32, 0x40000
	s_addc_u32 s35, s33, 0
	global_load_dwordx4 v[2:5], v1, s[34:35]
	global_load_dwordx4 v[6:9], v1, s[32:33]
	global_load_dwordx4 v[10:13], v1, s[30:31]
	global_load_dwordx4 v[14:17], v1, s[28:29]
	global_load_dwordx4 v[18:21], v1, s[26:27]
	global_load_dwordx4 v[22:25], v1, s[24:25]
	v_bfe_u32 v103, v0, 5, 1
	v_lshrrev_b32_e32 v33, 2, v0
	global_load_dwordx4 v[66:69], v1, s[22:23]
	global_load_dwordx4 v[74:77], v1, s[20:21]
	v_lshlrev_b32_e32 v104, 1, v78
	v_and_b32_e32 v27, 3, v0
	v_lshrrev_b32_e32 v28, 1, v0
	v_and_or_b32 v59, v33, 1, v104
	v_and_or_b32 v105, v28, 12, v27
	v_lshlrev_b32_e32 v28, 4, v103
	v_mov_b32_e32 v29, v32
	v_lshl_add_u64 v[56:57], s[6:7], 0, v[28:29]
	v_or_b32_e32 v27, s13, v59
	v_or_b32_e32 v28, s12, v105
	s_lshl_b32 s4, s16, 16
	v_lshl_add_u32 v31, v27, 7, v28
	s_or_b32 s2, s4, 0x4000
	v_add_u32_e32 v27, 0x400, v31
	s_or_b32 s5, s4, 0xc000
	v_add_u32_e32 v28, s2, v27
	v_and_b32_e32 v1, 31, v0
	v_ashrrev_i32_e32 v29, 31, v28
	v_add_u32_e32 v34, s5, v27
	v_or_b32_e32 v26, s15, v1
	v_lshlrev_b64 v[28:29], 5, v[28:29]
	v_ashrrev_i32_e32 v35, 31, v34
	v_lshl_add_u64 v[28:29], v[56:57], 0, v[28:29]
	v_lshlrev_b64 v[34:35], 5, v[34:35]
	v_lshl_or_b32 v58, v26, 1, v103
	v_lshl_add_u64 v[34:35], v[56:57], 0, v[34:35]
	global_load_dwordx4 v[36:39], v[28:29], off
	global_load_dwordx4 v[40:43], v[34:35], off
	v_add_u32_e32 v28, 0x180, v58
	v_ashrrev_i32_e32 v29, 31, v28
	v_add_u32_e32 v34, 0x480, v58
	v_lshl_add_u64 v[28:29], v[28:29], 4, s[8:9]
	v_ashrrev_i32_e32 v35, 31, v34
	v_ashrrev_i32_e32 v27, 31, v26
	v_lshl_add_u64 v[34:35], v[34:35], 4, s[8:9]
	global_load_dwordx4 v[44:47], v[28:29], off
	global_load_dwordx4 v[48:51], v[34:35], off
	v_lshl_add_u64 v[60:61], v[26:27], 2, s[10:11]
	v_add_u32_e32 v26, s5, v31
	v_add_u32_e32 v28, s2, v31
	v_ashrrev_i32_e32 v27, 31, v26
	v_ashrrev_i32_e32 v29, 31, v28
	v_lshlrev_b64 v[26:27], 5, v[26:27]
	v_lshlrev_b64 v[28:29], 5, v[28:29]
	global_load_dword v62, v[60:61], off offset:768
	global_load_dword v64, v[60:61], off offset:2304
	v_lshl_add_u64 v[26:27], v[56:57], 0, v[26:27]
	v_lshl_add_u64 v[28:29], v[56:57], 0, v[28:29]
	global_load_dwordx4 v[52:55], v[26:27], off
	s_nop 0
	global_load_dwordx4 v[26:29], v[28:29], off
	s_load_dwordx2 s[0:1], s[0:1], 0x28
	v_and_b32_e32 v0, 63, v0
	v_bfrev_b32_e32 v31, 60
	v_cmp_gt_u32_e32 vcc, 32, v0
	v_mul_u32_u24_e32 v102, 0x410, v1
	v_lshlrev_b32_e32 v0, 2, v1
	v_mov_b32_e32 v1, v32
	v_cndmask_b32_e64 v34, v31, 0, vcc
	s_waitcnt lgkmcnt(0)
	v_lshl_add_u64 v[72:73], s[0:1], 0, v[0:1]
	v_mul_u32_u24_e32 v0, 0x410, v78
	v_lshlrev_b32_e32 v1, 6, v65
	v_add3_u32 v1, v0, v1, v30
	s_mul_i32 s16, s16, 24
	s_lshr_b32 s0, s15, 5
	s_waitcnt vmcnt(8)
	ds_write_b128 v1, v[74:77]
	ds_write_b128 v1, v[66:69] offset:4160
	ds_write_b128 v1, v[22:25] offset:8320
	ds_write_b128 v1, v[18:21] offset:12480
	ds_write_b128 v1, v[14:17] offset:16640
	ds_write_b128 v1, v[10:13] offset:20800
	ds_write_b128 v1, v[6:9] offset:24960
	ds_write_b128 v1, v[2:5] offset:29120
	s_add_i32 s0, s0, s16
	s_waitcnt lgkmcnt(0)
	s_barrier
	s_lshl_b32 s2, s0, 10
	v_mov_b32_e32 v33, v32
	v_mov_b32_e32 v35, v32
	v_lshl_or_b32 v106, v103, 2, v102
	s_add_i32 s5, s2, 0x4800
	v_or_b32_e32 v107, s13, v103
	s_ashr_i32 s6, s14, 3
	s_add_i32 s7, s2, 0x1800
	s_mov_b64 s[0:1], -1
	s_mov_b32 s10, 0x7f61b1e6
	s_mov_b32 s11, 0x42800000
	s_waitcnt vmcnt(3)
	v_mov_b32_e32 v63, v62
	s_waitcnt vmcnt(2)
	v_mov_b32_e32 v65, v64
	s_waitcnt vmcnt(0)
	s_branch .LBB2_3
